# barrier-time conversion with 3 waves per workgroup (waves 1-3) at barriers 0-9, plus static prio for waves 4-7 in attention
# baseline (speedup 1.0000x reference)
.LBB0_164:
	s_or_b64 exec, exec, s[0:1]
	s_cmp_lg_u32 s15, 0x100
	s_cbranch_scc1 .Lbtc_skip_0
	s_lshr_b32 s98, s81, 6
	s_cmp_eq_u32 s98, 0
	s_cbranch_scc1 .Lbtc_skip_0
	s_cmp_gt_u32 s98, 3
	s_cbranch_scc1 .Lbtc_skip_0
	v_writelane_b32 v255, s80, 2
	v_writelane_b32 v255, s81, 3
	v_writelane_b32 v255, s82, 4
	s_mov_b32 s99, 1
	s_mul_i32 s100, s14, 3
	s_add_i32 s100, s100, s98
	s_add_i32 s100, s100, 8631
	s_mov_b32 s41, s14
	s_mov_b32 s47, s81
	s_mov_b64 s[6:7], s[34:35]
	v_mbcnt_hi_u32_b32 v184, -1, v253
	s_and_b32 s0, s81, 0xffffffc0
	v_add_u32_e32 v184, s0, v184
	s_branch .Lbtc_entry

.LBB0_223:
	s_or_b64 exec, exec, s[0:1]
	s_cmp_lg_u32 s15, 0x100
	s_cbranch_scc1 .Lbtc_skip_1
	s_lshr_b32 s98, s81, 6
	s_cmp_eq_u32 s98, 0
	s_cbranch_scc1 .Lbtc_skip_1
	s_cmp_gt_u32 s98, 3
	s_cbranch_scc1 .Lbtc_skip_1
	v_writelane_b32 v255, s80, 2
	v_writelane_b32 v255, s81, 3
	v_writelane_b32 v255, s82, 4
	s_mov_b32 s99, 2
	s_mul_i32 s100, s14, 3
	s_add_i32 s100, s100, s98
	s_add_i32 s100, s100, 9399
	s_mov_b32 s41, s14
	s_mov_b32 s47, s81
	s_mov_b64 s[6:7], s[34:35]
	v_mbcnt_hi_u32_b32 v184, -1, v253
	s_and_b32 s0, s81, 0xffffffc0
	v_add_u32_e32 v184, s0, v184
	s_branch .Lbtc_entry

.LBB0_354:
	s_or_b64 exec, exec, s[0:1]
	s_cmp_lg_u32 s15, 0x100
	s_cbranch_scc1 .Lbtc_skip_2
	s_lshr_b32 s98, s81, 6
	s_cmp_eq_u32 s98, 0
	s_cbranch_scc1 .Lbtc_skip_2
	s_cmp_gt_u32 s98, 3
	s_cbranch_scc1 .Lbtc_skip_2
	v_writelane_b32 v255, s80, 2
	v_writelane_b32 v255, s81, 3
	v_writelane_b32 v255, s82, 4
	s_mov_b32 s99, 3
	s_mul_i32 s100, s14, 3
	s_add_i32 s100, s100, s98
	s_add_i32 s100, s100, 10167
	s_mov_b32 s41, s14
	s_mov_b32 s47, s81
	s_mov_b64 s[6:7], s[34:35]
	v_mbcnt_hi_u32_b32 v184, -1, v253
	s_and_b32 s0, s81, 0xffffffc0
	v_add_u32_e32 v184, s0, v184
	s_branch .Lbtc_entry

.LBB0_457:
	s_or_b64 exec, exec, s[0:1]
	s_cmp_lg_u32 s15, 0x100
	s_cbranch_scc1 .Lbtc_skip_3
	s_lshr_b32 s98, s81, 6
	s_cmp_eq_u32 s98, 0
	s_cbranch_scc1 .Lbtc_skip_3
	s_cmp_gt_u32 s98, 3
	s_cbranch_scc1 .Lbtc_skip_3
	v_writelane_b32 v255, s80, 2
	v_writelane_b32 v255, s81, 3
	v_writelane_b32 v255, s82, 4
	s_mov_b32 s99, 4
	s_mul_i32 s100, s14, 3
	s_add_i32 s100, s100, s98
	s_add_i32 s100, s100, 10935
	s_mov_b32 s41, s14
	s_mov_b32 s47, s81
	s_mov_b64 s[6:7], s[34:35]
	v_mbcnt_hi_u32_b32 v184, -1, v253
	s_and_b32 s0, s81, 0xffffffc0
	v_add_u32_e32 v184, s0, v184
	s_branch .Lbtc_entry

.LBB0_543:
	s_or_b64 exec, exec, s[0:1]
	s_cmp_lg_u32 s15, 0x100
	s_cbranch_scc1 .Lbtc_skip_4
	s_lshr_b32 s98, s81, 6
	s_cmp_eq_u32 s98, 0
	s_cbranch_scc1 .Lbtc_skip_4
	s_cmp_gt_u32 s98, 3
	s_cbranch_scc1 .Lbtc_skip_4
	v_writelane_b32 v255, s80, 2
	v_writelane_b32 v255, s81, 3
	v_writelane_b32 v255, s82, 4
	s_mov_b32 s99, 5
	s_mul_i32 s100, s14, 3
	s_add_i32 s100, s100, s98
	s_add_i32 s100, s100, 11703
	s_mov_b32 s41, s14
	s_mov_b32 s47, s81
	s_mov_b64 s[6:7], s[34:35]
	v_mbcnt_hi_u32_b32 v184, -1, v253
	s_and_b32 s0, s81, 0xffffffc0
	v_add_u32_e32 v184, s0, v184
	s_branch .Lbtc_entry

.LBB0_894:
	s_or_b64 exec, exec, s[0:1]
	s_cmp_lg_u32 s15, 0x100
	s_cbranch_scc1 .Lbtc_skip_5
	s_lshr_b32 s98, s81, 6
	s_cmp_eq_u32 s98, 0
	s_cbranch_scc1 .Lbtc_skip_5
	s_cmp_gt_u32 s98, 3
	s_cbranch_scc1 .Lbtc_skip_5
	v_writelane_b32 v255, s80, 2
	v_writelane_b32 v255, s81, 3
	v_writelane_b32 v255, s82, 4
	s_mov_b32 s99, 6
	s_mul_i32 s100, s14, 3
	s_add_i32 s100, s100, s98
	s_add_i32 s100, s100, 12471
	s_mov_b32 s41, s14
	s_mov_b32 s47, s81
	s_mov_b64 s[6:7], s[34:35]
	v_mbcnt_hi_u32_b32 v184, -1, v253
	s_and_b32 s0, s81, 0xffffffc0
	v_add_u32_e32 v184, s0, v184
	s_branch .Lbtc_entry

.LBB0_968:
	s_or_b64 exec, exec, s[0:1]
	s_cmp_lg_u32 s15, 0x100
	s_cbranch_scc1 .Lbtc_skip_6
	s_lshr_b32 s98, s81, 6
	s_cmp_eq_u32 s98, 0
	s_cbranch_scc1 .Lbtc_skip_6
	s_cmp_gt_u32 s98, 3
	s_cbranch_scc1 .Lbtc_skip_6
	v_writelane_b32 v255, s80, 2
	v_writelane_b32 v255, s81, 3
	v_writelane_b32 v255, s82, 4
	s_mov_b32 s99, 7
	s_mul_i32 s100, s14, 3
	s_add_i32 s100, s100, s98
	s_add_i32 s100, s100, 13239
	s_mov_b32 s41, s14
	s_mov_b32 s47, s81
	s_mov_b64 s[6:7], s[34:35]
	v_mbcnt_hi_u32_b32 v184, -1, v253
	s_and_b32 s0, s81, 0xffffffc0
	v_add_u32_e32 v184, s0, v184
	s_branch .Lbtc_entry

.LBB0_1042:
	s_or_b64 exec, exec, s[0:1]
	s_cmp_lg_u32 s15, 0x100
	s_cbranch_scc1 .Lbtc_skip_7
	s_lshr_b32 s98, s81, 6
	s_cmp_eq_u32 s98, 0
	s_cbranch_scc1 .Lbtc_skip_7
	s_cmp_gt_u32 s98, 3
	s_cbranch_scc1 .Lbtc_skip_7
	v_writelane_b32 v255, s80, 2
	v_writelane_b32 v255, s81, 3
	v_writelane_b32 v255, s82, 4
	s_mov_b32 s99, 8
	s_mul_i32 s100, s14, 3
	s_add_i32 s100, s100, s98
	s_add_i32 s100, s100, 14007
	s_mov_b32 s41, s14
	s_mov_b32 s47, s81
	s_mov_b64 s[6:7], s[34:35]
	v_mbcnt_hi_u32_b32 v184, -1, v253
	s_and_b32 s0, s81, 0xffffffc0
	v_add_u32_e32 v184, s0, v184
	s_branch .Lbtc_entry

.LBB0_1058:
	s_add_i32 s1, s40, 0xffffff78
	s_lshl_b32 s0, s38, 3
	s_max_i32 s1, s1, 0
	s_mulk_i32 s1, 0x48
	s_cmp_eq_u32 s40, 0x100
	s_cselect_b32 s98, 6144, 0
	s_add_i32 s1, s1, s98
	s_add_i32 s0, s42, s0
	s_add_i32 s43, s0, s1
	s_cmpk_gt_i32 s43, 0x5fff
	s_mov_b32 s1, 0
	s_cbranch_scc1 .LBB0_1135
	s_lshl_b32 s44, s40, 3
	s_add_u32 s45, s10, 0x17458000
	s_mul_i32 s0, s42, 0x2400
	s_addc_u32 s46, s11, 0
	s_add_i32 s0, s0, 0
	s_add_u32 s47, s10, 0x7458000
	s_addc_u32 s48, s11, 0
	s_add_u32 s49, s10, 0x6458000
	s_addc_u32 s50, s11, 0
	s_add_u32 s51, s10, 0x5458000
	s_addc_u32 s52, s11, 0
	s_add_u32 s53, s10, 0x4d58000
	s_addc_u32 s54, s11, 0
	s_add_u32 s55, s10, 0x158000
	s_addc_u32 s56, s11, 0
	s_add_u32 s57, s10, 0x3390c000
	s_addc_u32 s58, s11, 0
	s_add_u32 s59, s10, 0x35e0c000
	v_lshlrev_b32_e32 v2, 1, v86
	v_and_b32_e32 v0, 60, v0
	v_and_b32_e32 v80, 48, v54
	s_addc_u32 s60, s11, 0
	v_and_b32_e32 v2, 0x60, v2
	v_and_b32_e32 v8, 7, v85
	v_lshrrev_b32_e32 v90, 3, v86
	v_mov_b32_e32 v79, 0
	v_add_u32_e32 v1, s0, v76
	v_mul_u32_u24_e32 v3, 0x50, v0
	v_add_u32_e32 v4, s0, v80
	v_mul_u32_u24_e32 v5, 0x50, v87
	s_add_u32 s61, s10, 0x3760c000
	v_add_u32_e32 v6, s0, v2
	v_mul_u32_u24_e32 v7, 0x90, v0
	v_lshlrev_b32_e32 v2, 3, v8
	v_lshl_add_u32 v8, v8, 4, s0
	v_mul_u32_u24_e32 v9, 0x90, v90
	v_mov_b32_e32 v81, v79
	v_or_b32_e32 v77, 16, v87
	v_or_b32_e32 v88, 32, v87
	v_or_b32_e32 v89, 48, v87
	s_addc_u32 s62, s11, 0
	v_or_b32_e32 v91, 8, v90
	v_or_b32_e32 v92, 16, v90
	v_or_b32_e32 v93, 24, v90
	v_or_b32_e32 v94, 32, v90
	v_or_b32_e32 v95, 40, v90
	v_or_b32_e32 v96, 48, v90
	v_or_b32_e32 v97, 56, v90
	s_add_i32 s63, 0, 0x204f8
	s_movk_i32 s64, 0x2000
	s_movk_i32 s65, 0x4000
	s_movk_i32 s66, 0x6000
	s_mov_b32 s67, 0x12000
	s_mov_b32 s68, 0xc3e00000
	v_add_u32_e32 v98, v1, v3
	v_add_u32_e32 v99, v4, v5
	s_movk_i32 s69, 0x3000
	s_movk_i32 s70, 0x5000
	s_movk_i32 s71, 0x7000
	s_add_i32 s72, 0, 0x204c0
	s_add_i32 s73, 0, 0x204b8
	s_add_i32 s74, 0, 0x204b0
	s_add_i32 s75, 0, 0x204a8
	s_add_i32 s76, 0, 0x20458
	s_add_i32 s77, 0, 0x20448
	s_add_i32 s78, 0, 0x20440
	s_mov_b32 s79, 0x9000
	s_mov_b32 s80, 0x1b000
	s_mov_b32 s81, 0x25000
	s_mov_b32 s82, 0x2e000
	s_mov_b32 s83, 0x37000
	s_mov_b32 s84, 0x41000
	s_mov_b32 s85, 0x4a000
	s_mov_b32 s86, 0x53000
	s_mov_b32 s87, 0x5d000
	s_mov_b32 s88, 0x66000
	s_mov_b32 s89, 0x6f000
	s_mov_b32 s90, 0x79000
	s_mov_b32 s91, 0x82000
	s_mov_b32 s92, 0x8b000
	v_add_u32_e32 v100, v6, v7
	v_lshlrev_b32_e32 v78, 1, v2
	v_lshlrev_b32_e32 v82, 2, v0
	v_mov_b32_e32 v101, 0x43e00000
	v_mov_b32_e32 v104, v79
	v_mov_b32_e32 v105, v79
	v_mov_b32_e32 v106, v79
	v_mov_b32_e32 v107, v79
	v_add_u32_e32 v102, v8, v9
	s_branch .LBB0_1062

.LBB0_1197:
	s_or_b64 exec, exec, s[0:1]
	s_cmp_lg_u32 s15, 0x100
	s_cbranch_scc1 .Lbtc_skip_8
	s_lshr_b32 s98, s81, 6
	s_cmp_eq_u32 s98, 0
	s_cbranch_scc1 .Lbtc_skip_8
	s_cmp_gt_u32 s98, 3
	s_cbranch_scc1 .Lbtc_skip_8
	v_writelane_b32 v255, s80, 2
	v_writelane_b32 v255, s81, 3
	v_writelane_b32 v255, s82, 4
	s_mov_b32 s99, 9
	s_mul_i32 s100, s14, 3
	s_add_i32 s100, s100, s98
	s_add_i32 s100, s100, 24567
	s_mov_b32 s41, s14
	s_mov_b32 s47, s81
	s_mov_b64 s[6:7], s[34:35]
	v_mbcnt_hi_u32_b32 v184, -1, v253
	s_and_b32 s0, s81, 0xffffffc0
	v_add_u32_e32 v184, s0, v184
	s_branch .Lbtc_entry

.LBB0_1341:
	s_or_b64 exec, exec, s[0:1]
	s_cmp_lg_u32 s15, 0x100
	s_cbranch_scc1 .Lbtc_skip_9
	s_lshr_b32 s98, s81, 6
	s_cmp_eq_u32 s98, 0
	s_cbranch_scc1 .Lbtc_skip_9
	s_cmp_gt_u32 s98, 3
	s_cbranch_scc1 .Lbtc_skip_9
	v_writelane_b32 v255, s80, 2
	v_writelane_b32 v255, s81, 3
	v_writelane_b32 v255, s82, 4
	s_mov_b32 s99, 10
	s_mul_i32 s100, s14, 3
	s_add_i32 s100, s100, s98
	s_add_i32 s100, s100, 25335
	s_mov_b32 s41, s14
	s_mov_b32 s47, s81
	s_mov_b64 s[6:7], s[34:35]
	v_mbcnt_hi_u32_b32 v184, -1, v253
	s_and_b32 s0, s81, 0xffffffc0
	v_add_u32_e32 v184, s0, v184
	s_branch .Lbtc_entry

.LBB0_1412:
	s_cmpk_lt_i32 s4, 0x1cc0
	s_barrier
	s_cbranch_scc0 .LBB0_1489
	s_add_u32 s3, s0, 0x17458000
	s_mulk_i32 s12, 0x2400
	s_addc_u32 s40, s1, 0
	s_add_i32 s6, s12, 0
	s_add_u32 s41, s0, 0x7458000
	s_addc_u32 s42, s1, 0
	s_add_u32 s43, s0, 0x6458000
	s_addc_u32 s44, s1, 0
	s_add_u32 s45, s0, 0x5458000
	s_addc_u32 s46, s1, 0
	s_add_u32 s47, s0, 0x4d58000
	s_addc_u32 s48, s1, 0
	s_add_u32 s49, s0, 0x158000
	s_addc_u32 s50, s1, 0
	s_add_u32 s51, s0, 0x3390c000
	s_addc_u32 s52, s1, 0
	s_add_u32 s53, s0, 0x35e0c000
	v_lshlrev_b32_e32 v7, 1, v1
	v_and_b32_e32 v75, 48, v0
	v_and_b32_e32 v2, 60, v2
	v_and_b32_e32 v70, 48, v3
	v_lshrrev_b32_e32 v76, 2, v1
	s_addc_u32 s54, s1, 0
	v_and_b32_e32 v7, 0x60, v7
	v_and_b32_e32 v9, 7, v0
	v_lshrrev_b32_e32 v80, 3, v1
	v_mov_b32_e32 v69, 0
	v_add_u32_e32 v4, s6, v75
	v_mul_u32_u24_e32 v5, 0x50, v2
	v_add_u32_e32 v3, s6, v70
	v_mul_u32_u24_e32 v6, 0x50, v76
	s_add_u32 s55, s0, 0x3760c000
	v_add_u32_e32 v7, s6, v7
	v_mul_u32_u24_e32 v8, 0x90, v2
	v_lshlrev_b32_e32 v0, 3, v9
	v_lshl_add_u32 v9, v9, 4, s6
	v_mul_u32_u24_e32 v1, 0x90, v80
	s_mov_b32 s5, 0
	v_mov_b32_e32 v71, v69
	v_or_b32_e32 v77, 16, v76
	v_or_b32_e32 v78, 32, v76
	v_or_b32_e32 v79, 48, v76
	s_addc_u32 s56, s1, 0
	v_or_b32_e32 v81, 8, v80
	v_or_b32_e32 v82, 16, v80
	v_or_b32_e32 v83, 24, v80
	v_or_b32_e32 v84, 32, v80
	v_or_b32_e32 v85, 40, v80
	v_or_b32_e32 v86, 48, v80
	v_or_b32_e32 v87, 56, v80
	s_add_i32 s57, s4, 0xf97f
	s_cmp_eq_u32 s15, 0x100
	s_cselect_b32 s98, 1536, 0
	s_add_i32 s57, s57, s98
	s_add_i32 s58, 0, 0x204f8
	s_movk_i32 s59, 0x2000
	s_movk_i32 s60, 0x4000
	s_movk_i32 s61, 0x6000
	s_mov_b32 s62, 0x12000
	s_mov_b32 s63, 0x18000
	s_mov_b32 s64, 0x1a000
	s_mov_b32 s65, 0x1c000
	s_mov_b32 s66, 0x1e000
	s_mov_b32 s67, 0xc3e00000
	v_add_u32_e32 v88, v4, v5
	v_add_u32_e32 v89, v3, v6
	s_movk_i32 s68, 0x1000
	s_movk_i32 s69, 0x3000
	s_movk_i32 s70, 0x5000
	s_movk_i32 s71, 0x7000
	s_add_i32 s72, 0, 0x204c0
	s_add_i32 s73, 0, 0x204b8
	s_add_i32 s74, 0, 0x204b0
	s_add_i32 s75, 0, 0x204a8
	s_add_i32 s76, 0, 0x20458
	s_add_i32 s77, 0, 0x20448
	s_add_i32 s78, 0, 0x20440
	s_mov_b32 s79, 0x9000
	s_mov_b32 s80, 0x1b000
	s_mov_b32 s81, 0x25000
	s_mov_b32 s82, 0x2e000
	s_mov_b32 s83, 0x37000
	s_mov_b32 s84, 0x41000
	s_mov_b32 s85, 0x4a000
	s_mov_b32 s86, 0x53000
	s_mov_b32 s87, 0x5d000
	s_mov_b32 s88, 0x66000
	s_mov_b32 s89, 0x6f000
	s_mov_b32 s90, 0x79000
	s_mov_b32 s91, 0x82000
	s_mov_b32 s92, 0x8b000
	v_add_u32_e32 v90, v7, v8
	v_lshlrev_b32_e32 v68, 1, v0
	v_lshlrev_b32_e32 v72, 2, v2
	v_mov_b32_e32 v91, 0x43e00000
	v_mov_b32_e32 v94, v69
	v_mov_b32_e32 v95, v69
	v_mov_b32_e32 v96, v69
	v_mov_b32_e32 v97, v69
	v_add_u32_e32 v92, v9, v1
	s_branch .LBB0_1416
